# fp8 kernels phases 1 and 5: last four A-fragment LDS reads issued behind the first MFMA of the compute segment, pre-barrier wait lgkmcnt(4)
# speedup vs baseline: 1.0045x; 1.0045x over previous
.LBB3_4:
	ds_read_b128 v[2:5], v203
	ds_read_b128 v[10:13], v203 offset:2048
	ds_read_b128 v[6:9], v204
	ds_read_b128 v[14:17], v204 offset:2048
	s_mov_b32 m0, s46
	ds_read_b128 v[58:61], v200
	ds_read_b128 v[50:53], v200 offset:2048
	ds_read_b128 v[62:65], v201
	ds_read_b128 v[54:57], v201 offset:2048
	buffer_load_dwordx4 v1, s[12:15], 0 offen lds
	s_mov_b32 m0, s47
	s_nop 0
	buffer_load_dwordx4 v195, s[12:15], 0 offen lds
	s_waitcnt lgkmcnt(4)
	s_barrier
	s_waitcnt lgkmcnt(0)
	s_setprio 1
	v_mfma_f32_16x16x128_f8f6f4 v[190:193], v[2:9], v[58:65], v[190:193]
	ds_read_b128 v[42:45], v200 offset:4096
	ds_read_b128 v[34:37], v200 offset:6144
	ds_read_b128 v[46:49], v201 offset:4096
	ds_read_b128 v[38:41], v201 offset:6144
	v_mfma_f32_16x16x128_f8f6f4 v[186:189], v[10:17], v[58:65], v[186:189]
	v_mfma_f32_16x16x128_f8f6f4 v[174:177], v[2:9], v[50:57], v[174:177]
	v_mfma_f32_16x16x128_f8f6f4 v[170:173], v[10:17], v[50:57], v[170:173]
	s_waitcnt lgkmcnt(0)
	v_mfma_f32_16x16x128_f8f6f4 v[158:161], v[2:9], v[42:49], v[158:161]
	v_mfma_f32_16x16x128_f8f6f4 v[154:157], v[10:17], v[42:49], v[154:157]
	v_mfma_f32_16x16x128_f8f6f4 v[142:145], v[2:9], v[34:41], v[142:145]
	v_mfma_f32_16x16x128_f8f6f4 v[138:141], v[10:17], v[34:41], v[138:141]
	s_setprio 0
	s_barrier
	ds_read_b128 v[26:29], v205
	ds_read_b128 v[18:21], v205 offset:2048
	ds_read_b128 v[30:33], v206
	ds_read_b128 v[22:25], v206 offset:2048
	s_and_b64 vcc, exec, s[18:19]
	s_cbranch_vccnz .LBB3_6
	s_and_b32 s21, s53, 0xffff
	s_mov_b32 s22, s14
	s_mov_b32 s23, s15
	s_mov_b32 m0, s33
	s_nop 0
	buffer_load_dwordx4 v194, s[20:23], 0 offen lds
	s_mov_b32 m0, s34
	s_nop 0
	buffer_load_dwordx4 v196, s[20:23], 0 offen lds

.LBB3_12:
	s_barrier
	s_setprio 1
	v_mfma_f32_16x16x128_f8f6f4 v[118:121], v[26:33], v[58:65], v[118:121]
	s_add_i32 s13, 0, 0x18000
	v_add_u32_e32 v2, s13, v198
	v_add_u32_e32 v6, s13, v199
	v_mfma_f32_16x16x128_f8f6f4 v[114:117], v[18:25], v[58:65], v[114:117]
	v_mfma_f32_16x16x128_f8f6f4 v[102:105], v[26:33], v[50:57], v[102:105]
	v_mfma_f32_16x16x128_f8f6f4 v[98:101], v[18:25], v[50:57], v[98:101]
	v_mfma_f32_16x16x128_f8f6f4 v[86:89], v[26:33], v[42:49], v[86:89]
	v_mfma_f32_16x16x128_f8f6f4 v[82:85], v[18:25], v[42:49], v[82:85]
	v_mfma_f32_16x16x128_f8f6f4 v[70:73], v[26:33], v[34:41], v[70:73]
	v_mfma_f32_16x16x128_f8f6f4 v[66:69], v[18:25], v[34:41], v[66:69]
	s_setprio 0
	s_barrier
	ds_read_b128 v[10:13], v2
	ds_read_b128 v[2:5], v2 offset:2048
	ds_read_b128 v[14:17], v6
	ds_read_b128 v[6:9], v6 offset:2048
	ds_read_b128 v[58:61], v200 offset:32768
	ds_read_b128 v[50:53], v200 offset:34816
	ds_read_b128 v[62:65], v201 offset:32768
	ds_read_b128 v[54:57], v201 offset:34816
	s_and_b64 vcc, exec, s[0:1]
	s_cbranch_vccnz .LBB3_14
	s_add_u32 s56, s54, 0x100100
	s_addc_u32 s13, s55, 0
	s_and_b32 s57, s13, 0xffff
	s_mov_b32 s58, s14
	s_mov_b32 s59, s15
	s_mov_b32 m0, s37
	s_nop 0
	buffer_load_dwordx4 v1, s[56:59], 0 offen lds
	s_mov_b32 m0, s38
	s_nop 0
	buffer_load_dwordx4 v195, s[56:59], 0 offen lds
.LBB3_14:
	s_waitcnt lgkmcnt(4)
	s_barrier
	s_waitcnt lgkmcnt(0)
	s_setprio 1
	v_mfma_f32_16x16x128_f8f6f4 v[190:193], v[10:17], v[58:65], v[190:193]
	ds_read_b128 v[42:45], v200 offset:36864
	ds_read_b128 v[34:37], v200 offset:38912
	ds_read_b128 v[46:49], v201 offset:36864
	ds_read_b128 v[38:41], v201 offset:38912
	v_mfma_f32_16x16x128_f8f6f4 v[186:189], v[2:9], v[58:65], v[186:189]
	v_mfma_f32_16x16x128_f8f6f4 v[174:177], v[10:17], v[50:57], v[174:177]
	v_mfma_f32_16x16x128_f8f6f4 v[170:173], v[2:9], v[50:57], v[170:173]
	s_waitcnt lgkmcnt(0)
	v_mfma_f32_16x16x128_f8f6f4 v[158:161], v[10:17], v[42:49], v[158:161]
	v_mfma_f32_16x16x128_f8f6f4 v[154:157], v[2:9], v[42:49], v[154:157]
	v_mfma_f32_16x16x128_f8f6f4 v[142:145], v[10:17], v[34:41], v[142:145]
	v_mfma_f32_16x16x128_f8f6f4 v[138:141], v[2:9], v[34:41], v[138:141]
	s_setprio 0
	s_barrier
	s_add_i32 s13, 0, 0x1c000
	v_add_u32_e32 v18, s13, v198
	v_add_u32_e32 v22, s13, v199
	ds_read_b128 v[26:29], v18
	ds_read_b128 v[18:21], v18 offset:2048
	ds_read_b128 v[30:33], v22
	ds_read_b128 v[22:25], v22 offset:2048
	s_and_b64 vcc, exec, s[0:1]
	s_cbranch_vccnz .LBB3_16
	s_and_b64 s[22:23], exec, s[18:19]
	s_cselect_b32 s20, s8, s20
	s_cselect_b32 s13, s25, s53
	s_add_u32 s56, s20, 0x80
	s_addc_u32 s13, s13, 0
	s_and_b32 s57, s13, 0xffff
	s_mov_b32 s58, s14
	s_mov_b32 s59, s15
	s_mov_b32 m0, s40
	s_nop 0
	buffer_load_dwordx4 v194, s[56:59], 0 offen lds
	s_mov_b32 m0, s41
	s_nop 0
	buffer_load_dwordx4 v196, s[56:59], 0 offen lds

.LBB4_14:
	ds_read_b128 v[0:3], v202
	ds_read_b128 v[8:11], v202 offset:2048
	ds_read_b128 v[4:7], v203
	ds_read_b128 v[12:15], v203 offset:2048
	s_mov_b32 m0, s42
	ds_read_b128 v[56:59], v200
	ds_read_b128 v[48:51], v200 offset:2048
	ds_read_b128 v[60:63], v201
	ds_read_b128 v[52:55], v201 offset:2048
	buffer_load_dwordx4 v192, s[12:15], 0 offen lds
	s_mov_b32 m0, s43
	s_nop 0
	buffer_load_dwordx4 v194, s[12:15], 0 offen lds
	s_waitcnt lgkmcnt(4)
	s_barrier
	s_waitcnt lgkmcnt(0)
	s_setprio 1
	v_mfma_f32_16x16x128_f8f6f4 v[188:191], v[0:7], v[56:63], v[188:191]
	ds_read_b128 v[40:43], v200 offset:4096
	ds_read_b128 v[32:35], v200 offset:6144
	ds_read_b128 v[44:47], v201 offset:4096
	ds_read_b128 v[36:39], v201 offset:6144
	v_mfma_f32_16x16x128_f8f6f4 v[184:187], v[8:15], v[56:63], v[184:187]
	v_mfma_f32_16x16x128_f8f6f4 v[172:175], v[0:7], v[48:55], v[172:175]
	v_mfma_f32_16x16x128_f8f6f4 v[168:171], v[8:15], v[48:55], v[168:171]
	s_waitcnt lgkmcnt(0)
	v_mfma_f32_16x16x128_f8f6f4 v[156:159], v[0:7], v[40:47], v[156:159]
	v_mfma_f32_16x16x128_f8f6f4 v[152:155], v[8:15], v[40:47], v[152:155]
	v_mfma_f32_16x16x128_f8f6f4 v[140:143], v[0:7], v[32:39], v[140:143]
	v_mfma_f32_16x16x128_f8f6f4 v[136:139], v[8:15], v[32:39], v[136:139]
	s_setprio 0
	s_barrier
	ds_read_b128 v[24:27], v204
	ds_read_b128 v[16:19], v204 offset:2048
	ds_read_b128 v[28:31], v205
	ds_read_b128 v[20:23], v205 offset:2048
	s_and_b64 vcc, exec, s[18:19]
	s_cbranch_vccnz .LBB4_16
	s_and_b32 s21, s48, 0xffff
	s_mov_b32 s22, s14
	s_mov_b32 s23, s15
	s_mov_b32 m0, s28
	s_nop 0
	buffer_load_dwordx4 v193, s[20:23], 0 offen lds
	s_mov_b32 m0, s29
	s_nop 0
	buffer_load_dwordx4 v195, s[20:23], 0 offen lds

.LBB4_22:
	s_barrier
	s_setprio 1
	v_mfma_f32_16x16x128_f8f6f4 v[116:119], v[24:31], v[56:63], v[116:119]
	v_add_u32_e32 v0, s45, v198
	v_add_u32_e32 v4, s45, v199
	v_mfma_f32_16x16x128_f8f6f4 v[112:115], v[16:23], v[56:63], v[112:115]
	v_mfma_f32_16x16x128_f8f6f4 v[100:103], v[24:31], v[48:55], v[100:103]
	v_mfma_f32_16x16x128_f8f6f4 v[96:99], v[16:23], v[48:55], v[96:99]
	v_mfma_f32_16x16x128_f8f6f4 v[84:87], v[24:31], v[40:47], v[84:87]
	v_mfma_f32_16x16x128_f8f6f4 v[80:83], v[16:23], v[40:47], v[80:83]
	v_mfma_f32_16x16x128_f8f6f4 v[68:71], v[24:31], v[32:39], v[68:71]
	v_mfma_f32_16x16x128_f8f6f4 v[64:67], v[16:23], v[32:39], v[64:67]
	s_setprio 0
	s_barrier
	ds_read_b128 v[8:11], v0
	ds_read_b128 v[0:3], v0 offset:2048
	ds_read_b128 v[12:15], v4
	ds_read_b128 v[4:7], v4 offset:2048
	ds_read_b128 v[56:59], v200 offset:32768
	ds_read_b128 v[48:51], v200 offset:34816
	ds_read_b128 v[60:63], v201 offset:32768
	ds_read_b128 v[52:55], v201 offset:34816
	s_and_b64 vcc, exec, s[0:1]
	s_cbranch_vccnz .LBB4_24
	s_add_u32 s52, s49, 0x40100
	s_addc_u32 s13, s50, 0
	s_and_b32 s53, s13, 0xffff
	s_mov_b32 s54, s14
	s_mov_b32 s55, s15
	s_mov_b32 m0, s34
	s_nop 0
	buffer_load_dwordx4 v192, s[52:55], 0 offen lds
	s_mov_b32 m0, s35
	s_nop 0
	buffer_load_dwordx4 v194, s[52:55], 0 offen lds
.LBB4_24:
	s_waitcnt lgkmcnt(4)
	s_barrier
	s_waitcnt lgkmcnt(0)
	s_setprio 1
	v_mfma_f32_16x16x128_f8f6f4 v[188:191], v[8:15], v[56:63], v[188:191]
	ds_read_b128 v[40:43], v200 offset:36864
	ds_read_b128 v[32:35], v200 offset:38912
	ds_read_b128 v[44:47], v201 offset:36864
	ds_read_b128 v[36:39], v201 offset:38912
	v_mfma_f32_16x16x128_f8f6f4 v[184:187], v[0:7], v[56:63], v[184:187]
	v_mfma_f32_16x16x128_f8f6f4 v[172:175], v[8:15], v[48:55], v[172:175]
	v_mfma_f32_16x16x128_f8f6f4 v[168:171], v[0:7], v[48:55], v[168:171]
	s_waitcnt lgkmcnt(0)
	v_mfma_f32_16x16x128_f8f6f4 v[156:159], v[8:15], v[40:47], v[156:159]
	v_mfma_f32_16x16x128_f8f6f4 v[152:155], v[0:7], v[40:47], v[152:155]
	v_mfma_f32_16x16x128_f8f6f4 v[140:143], v[8:15], v[32:39], v[140:143]
	v_mfma_f32_16x16x128_f8f6f4 v[136:139], v[0:7], v[32:39], v[136:139]
	s_setprio 0
	s_barrier
	s_add_i32 s13, 0, 0x1c000
	v_add_u32_e32 v16, s13, v198
	v_add_u32_e32 v20, s13, v199
	ds_read_b128 v[24:27], v16
	ds_read_b128 v[16:19], v16 offset:2048
	ds_read_b128 v[28:31], v20
	ds_read_b128 v[20:23], v20 offset:2048
	s_and_b64 vcc, exec, s[0:1]
	s_cbranch_vccnz .LBB4_26
	s_and_b64 s[22:23], exec, s[18:19]
	s_cselect_b32 s20, s8, s20
	s_cselect_b32 s13, s3, s48
	s_add_u32 s48, s20, 0x80
	s_addc_u32 s13, s13, 0
	s_and_b32 s49, s13, 0xffff
	s_mov_b32 s50, s14
	s_mov_b32 s51, s15
	s_mov_b32 m0, s36
	s_nop 0
	buffer_load_dwordx4 v193, s[48:51], 0 offen lds
	s_mov_b32 m0, s37
	s_nop 0
	buffer_load_dwordx4 v195, s[48:51], 0 offen lds

.LBB5_18:
	ds_read_b128 v[0:3], v200
	ds_read_b128 v[8:11], v200 offset:2048
	ds_read_b128 v[4:7], v201
	ds_read_b128 v[12:15], v201 offset:2048
	s_mov_b32 m0, s43
	ds_read_b128 v[56:59], v198
	ds_read_b128 v[48:51], v198 offset:2048
	ds_read_b128 v[60:63], v199
	ds_read_b128 v[52:55], v199 offset:2048
	buffer_load_dwordx4 v192, s[8:11], 0 offen lds
	s_mov_b32 m0, s44
	s_nop 0
	buffer_load_dwordx4 v193, s[8:11], 0 offen lds
	s_waitcnt lgkmcnt(4)
	s_barrier
	s_waitcnt lgkmcnt(0)
	s_setprio 1
	v_mfma_f32_16x16x128_f8f6f4 v[188:191], v[0:7], v[56:63], v[188:191]
	ds_read_b128 v[40:43], v198 offset:4096
	ds_read_b128 v[32:35], v198 offset:6144
	ds_read_b128 v[44:47], v199 offset:4096
	ds_read_b128 v[36:39], v199 offset:6144
	v_mfma_f32_16x16x128_f8f6f4 v[184:187], v[8:15], v[56:63], v[184:187]
	v_mfma_f32_16x16x128_f8f6f4 v[176:179], v[0:7], v[48:55], v[176:179]
	v_mfma_f32_16x16x128_f8f6f4 v[168:171], v[8:15], v[48:55], v[168:171]
	s_waitcnt lgkmcnt(0)
	v_mfma_f32_16x16x128_f8f6f4 v[160:163], v[0:7], v[40:47], v[160:163]
	v_mfma_f32_16x16x128_f8f6f4 v[152:155], v[8:15], v[40:47], v[152:155]
	v_mfma_f32_16x16x128_f8f6f4 v[144:147], v[0:7], v[32:39], v[144:147]
	v_mfma_f32_16x16x128_f8f6f4 v[136:139], v[8:15], v[32:39], v[136:139]
	s_setprio 0
	s_barrier
	ds_read_b128 v[24:27], v202
	ds_read_b128 v[16:19], v202 offset:2048
	ds_read_b128 v[28:31], v203
	ds_read_b128 v[20:23], v203 offset:2048
	s_and_b64 vcc, exec, s[18:19]
	s_cbranch_vccnz .LBB5_20
	s_and_b32 s21, s49, 0xffff
	s_mov_b32 s22, s10
	s_mov_b32 s23, s11
	s_mov_b32 m0, s29
	s_nop 0
	buffer_load_dwordx4 v192, s[20:23], 0 offen lds
	s_mov_b32 m0, s30
	s_nop 0
	buffer_load_dwordx4 v193, s[20:23], 0 offen lds

.LBB5_26:
	s_barrier
	s_setprio 1
	v_mfma_f32_16x16x128_f8f6f4 v[108:111], v[24:31], v[56:63], v[108:111]
	v_add_u32_e32 v0, s46, v196
	v_add_u32_e32 v4, s46, v197
	v_mfma_f32_16x16x128_f8f6f4 v[104:107], v[16:23], v[56:63], v[104:107]
	v_mfma_f32_16x16x128_f8f6f4 v[92:95], v[24:31], v[48:55], v[92:95]
	v_mfma_f32_16x16x128_f8f6f4 v[88:91], v[16:23], v[48:55], v[88:91]
	v_mfma_f32_16x16x128_f8f6f4 v[80:83], v[24:31], v[40:47], v[80:83]
	v_mfma_f32_16x16x128_f8f6f4 v[76:79], v[16:23], v[40:47], v[76:79]
	v_mfma_f32_16x16x128_f8f6f4 v[68:71], v[24:31], v[32:39], v[68:71]
	v_mfma_f32_16x16x128_f8f6f4 v[64:67], v[16:23], v[32:39], v[64:67]
	s_setprio 0
	s_barrier
	ds_read_b128 v[8:11], v0
	ds_read_b128 v[0:3], v0 offset:2048
	ds_read_b128 v[12:15], v4
	ds_read_b128 v[4:7], v4 offset:2048
	ds_read_b128 v[56:59], v198 offset:32768
	ds_read_b128 v[48:51], v198 offset:34816
	ds_read_b128 v[60:63], v199 offset:32768
	ds_read_b128 v[52:55], v199 offset:34816
	s_and_b64 vcc, exec, s[0:1]
	s_cbranch_vccnz .LBB5_28
	s_add_u32 s52, s50, 0x40100
	s_addc_u32 s9, s51, 0
	s_and_b32 s53, s9, 0xffff
	s_mov_b32 s54, s10
	s_mov_b32 s55, s11
	s_mov_b32 m0, s34
	s_nop 0
	buffer_load_dwordx4 v192, s[52:55], 0 offen lds
	s_mov_b32 m0, s36
	s_nop 0
	buffer_load_dwordx4 v193, s[52:55], 0 offen lds
.LBB5_28:
	s_waitcnt lgkmcnt(4)
	s_barrier
	s_waitcnt lgkmcnt(0)
	s_setprio 1
	v_mfma_f32_16x16x128_f8f6f4 v[188:191], v[8:15], v[56:63], v[188:191]
	ds_read_b128 v[40:43], v198 offset:36864
	ds_read_b128 v[32:35], v198 offset:38912
	ds_read_b128 v[44:47], v199 offset:36864
	ds_read_b128 v[36:39], v199 offset:38912
	v_mfma_f32_16x16x128_f8f6f4 v[184:187], v[0:7], v[56:63], v[184:187]
	v_mfma_f32_16x16x128_f8f6f4 v[176:179], v[8:15], v[48:55], v[176:179]
	v_mfma_f32_16x16x128_f8f6f4 v[168:171], v[0:7], v[48:55], v[168:171]
	s_waitcnt lgkmcnt(0)
	v_mfma_f32_16x16x128_f8f6f4 v[160:163], v[8:15], v[40:47], v[160:163]
	v_mfma_f32_16x16x128_f8f6f4 v[152:155], v[0:7], v[40:47], v[152:155]
	v_mfma_f32_16x16x128_f8f6f4 v[144:147], v[8:15], v[32:39], v[144:147]
	v_mfma_f32_16x16x128_f8f6f4 v[136:139], v[0:7], v[32:39], v[136:139]
	s_setprio 0
	s_barrier
	s_add_i32 s9, 0, 0x1c000
	v_add_u32_e32 v16, s9, v196
	v_add_u32_e32 v20, s9, v197
	ds_read_b128 v[24:27], v16
	ds_read_b128 v[16:19], v16 offset:2048
	ds_read_b128 v[28:31], v20
	ds_read_b128 v[20:23], v20 offset:2048
	s_and_b64 vcc, exec, s[0:1]
	s_cbranch_vccnz .LBB5_30
	s_and_b64 s[22:23], exec, s[18:19]
	s_cselect_b32 s20, s12, s20
	s_cselect_b32 s9, s7, s49
	s_add_u32 s52, s20, 0x80
	s_addc_u32 s9, s9, 0
	s_and_b32 s53, s9, 0xffff
	s_mov_b32 s54, s10
	s_mov_b32 s55, s11
	s_mov_b32 m0, s37
	s_nop 0
	buffer_load_dwordx4 v192, s[52:55], 0 offen lds
	s_mov_b32 m0, s38
	s_nop 0
	buffer_load_dwordx4 v193, s[52:55], 0 offen lds
